# v5 attention: QK^T MFMAs chained 4-deep on one accumulator (kb; qb; c serpentine), PV serpentine
# speedup vs baseline: 1.0025x; 1.0025x over previous
.LBB0_734:
	s_waitcnt lgkmcnt(0)
	s_barrier
	ds_read_b128 v[160:163], v201 offset:0
	ds_read_b128 v[164:167], v202 offset:0
	ds_read_b128 v[168:171], v203 offset:0
	ds_read_b128 v[172:175], v204 offset:0
	ds_read_b128 v[176:179], v201 offset:4096
	ds_read_b128 v[180:183], v202 offset:4096
	ds_read_b128 v[230:233], v203 offset:4096
	ds_read_b128 v[234:237], v204 offset:4096
	s_waitcnt lgkmcnt(7)
	v_mfma_f32_16x16x32_bf16 v[64:67], v[160:163], v[96:99], 0
	s_waitcnt lgkmcnt(6)
	v_mfma_f32_16x16x32_bf16 v[64:67], v[164:167], v[100:103], v[64:67]
	s_add_u32 s16, s22, s10
	s_addc_u32 s17, s23, s11
	s_add_u32 s15, s22, s12
	s_addc_u32 s14, s23, s13
	s_add_u32 s8, s16, 0x3bc00200
	s_addc_u32 s9, s17, 0
	s_add_u32 s6, s15, 0x23a40000
	s_addc_u32 s7, s14, 0
	s_waitcnt lgkmcnt(5)
	v_mfma_f32_16x16x32_bf16 v[64:67], v[168:171], v[104:107], v[64:67]
	s_waitcnt lgkmcnt(4)
	v_mfma_f32_16x16x32_bf16 v[64:67], v[172:175], v[108:111], v[64:67]
	s_waitcnt vmcnt(4)
	ds_write_b128 v225, v[136:139] offset:32768
	v_mfma_f32_16x16x32_bf16 v[68:71], v[172:175], v[124:127], 0
	ds_read_b128 v[172:175], v204 offset:8192
	v_mfma_f32_16x16x32_bf16 v[68:71], v[168:171], v[120:123], v[68:71]
	ds_read_b128 v[168:171], v203 offset:8192
	ds_write_b128 v226, v[140:143] offset:32768
	v_mfma_f32_16x16x32_bf16 v[68:71], v[164:167], v[116:119], v[68:71]
	ds_read_b128 v[164:167], v202 offset:8192
	v_mfma_f32_16x16x32_bf16 v[68:71], v[160:163], v[112:115], v[68:71]
	ds_read_b128 v[160:163], v201 offset:8192
	ds_write_b64 v227, v[132:133] offset:32768
	s_waitcnt lgkmcnt(10)
	v_mfma_f32_16x16x32_bf16 v[72:75], v[176:179], v[96:99], 0
	s_waitcnt lgkmcnt(9)
	v_mfma_f32_16x16x32_bf16 v[72:75], v[180:183], v[100:103], v[72:75]
	ds_write_b64 v228, v[134:135] offset:32768
	s_waitcnt lgkmcnt(9)
	v_mfma_f32_16x16x32_bf16 v[72:75], v[230:233], v[104:107], v[72:75]
	s_waitcnt lgkmcnt(8)
	v_mfma_f32_16x16x32_bf16 v[72:75], v[234:237], v[108:111], v[72:75]
	ds_write_b64 v229, v[128:129] offset:32768
	v_mfma_f32_16x16x32_bf16 v[76:79], v[234:237], v[124:127], 0
	ds_read_b128 v[234:237], v204 offset:12288
	v_mfma_f32_16x16x32_bf16 v[76:79], v[230:233], v[120:123], v[76:79]
	ds_read_b128 v[230:233], v203 offset:12288
	ds_write_b64 v184, v[130:131] offset:32768
	v_mfma_f32_16x16x32_bf16 v[76:79], v[180:183], v[116:119], v[76:79]
	ds_read_b128 v[180:183], v202 offset:12288
	v_mfma_f32_16x16x32_bf16 v[76:79], v[176:179], v[112:115], v[76:79]
	ds_read_b128 v[176:179], v201 offset:12288
	global_load_dwordx4 v[132:135], v198, s[8:9]
	s_waitcnt lgkmcnt(8)
	v_mfma_f32_16x16x32_bf16 v[80:83], v[160:163], v[96:99], 0
	v_exp_f32_e32 v64, v64
	v_exp_f32_e32 v65, v65
	v_exp_f32_e32 v66, v66
	v_mfma_f32_16x16x32_bf16 v[80:83], v[164:167], v[100:103], v[80:83]
	v_exp_f32_e32 v67, v67
	v_exp_f32_e32 v68, v68
	v_exp_f32_e32 v69, v69
	global_load_dwordx4 v[128:131], v199, s[8:9]
	v_mfma_f32_16x16x32_bf16 v[80:83], v[168:171], v[104:107], v[80:83]
	v_exp_f32_e32 v70, v70
	v_exp_f32_e32 v71, v71
	v_add_f32_e32 v194, v194, v64
	v_mfma_f32_16x16x32_bf16 v[80:83], v[172:175], v[108:111], v[80:83]
	v_add_f32_e32 v194, v194, v65
	v_add_f32_e32 v194, v194, v66
	v_add_f32_e32 v194, v194, v67
	global_load_dwordx4 v[136:139], v196, s[6:7]
	v_mfma_f32_16x16x32_bf16 v[84:87], v[172:175], v[124:127], 0
	v_add_f32_e32 v195, v195, v68
	v_add_f32_e32 v195, v195, v69
	v_add_f32_e32 v195, v195, v70
	ds_read_b128 v[172:175], v209 offset:6144
	v_mfma_f32_16x16x32_bf16 v[84:87], v[168:171], v[120:123], v[84:87]
	v_add_f32_e32 v195, v195, v71
	v_cvt_pk_bf16_f32 v64, v64, v65
	v_cvt_pk_bf16_f32 v65, v66, v67
	ds_read_b128 v[168:171], v209 offset:4096
	global_load_dwordx4 v[140:143], v197, s[6:7]
	v_mfma_f32_16x16x32_bf16 v[84:87], v[164:167], v[116:119], v[84:87]
	v_cvt_pk_bf16_f32 v68, v68, v69
	v_cvt_pk_bf16_f32 v69, v70, v71
	ds_read_b128 v[164:167], v209 offset:2048
	v_mfma_f32_16x16x32_bf16 v[84:87], v[160:163], v[112:115], v[84:87]
	ds_read_b128 v[160:163], v209 offset:0
	s_waitcnt lgkmcnt(4)
	v_mfma_f32_16x16x32_bf16 v[88:91], v[176:179], v[96:99], 0
	v_exp_f32_e32 v72, v72
	v_exp_f32_e32 v73, v73
	v_exp_f32_e32 v74, v74
	v_mfma_f32_16x16x32_bf16 v[88:91], v[180:183], v[100:103], v[88:91]
	v_exp_f32_e32 v75, v75
	v_exp_f32_e32 v76, v76
	v_exp_f32_e32 v77, v77
	v_mfma_f32_16x16x32_bf16 v[88:91], v[230:233], v[104:107], v[88:91]
	v_exp_f32_e32 v78, v78
	v_exp_f32_e32 v79, v79
	v_add_f32_e32 v194, v194, v72
	v_mfma_f32_16x16x32_bf16 v[88:91], v[234:237], v[108:111], v[88:91]
	v_add_f32_e32 v194, v194, v73
	v_add_f32_e32 v194, v194, v74
	v_add_f32_e32 v194, v194, v75
	v_mfma_f32_16x16x32_bf16 v[92:95], v[234:237], v[124:127], 0
	v_add_f32_e32 v195, v195, v76
	v_add_f32_e32 v195, v195, v77
	v_add_f32_e32 v195, v195, v78
	ds_read_b128 v[234:237], v209 offset:14336
	v_mfma_f32_16x16x32_bf16 v[92:95], v[230:233], v[120:123], v[92:95]
	v_add_f32_e32 v195, v195, v79
	v_cvt_pk_bf16_f32 v66, v72, v73
	v_cvt_pk_bf16_f32 v67, v74, v75
	ds_read_b128 v[230:233], v209 offset:12288
	v_mfma_f32_16x16x32_bf16 v[92:95], v[180:183], v[116:119], v[92:95]
	v_cvt_pk_bf16_f32 v70, v76, v77
	v_cvt_pk_bf16_f32 v71, v78, v79
	ds_read_b128 v[180:183], v209 offset:10240
	v_mfma_f32_16x16x32_bf16 v[92:95], v[176:179], v[112:115], v[92:95]
	ds_read_b128 v[176:179], v209 offset:8192
	s_waitcnt lgkmcnt(4)
	v_mfma_f32_16x16x32_bf16 v[0:3], v[160:163], v[64:67], v[0:3]
	v_exp_f32_e32 v80, v80
	v_exp_f32_e32 v81, v81
	v_exp_f32_e32 v82, v82
	v_mfma_f32_16x16x32_bf16 v[4:7], v[160:163], v[68:71], v[4:7]
	v_exp_f32_e32 v83, v83
	v_exp_f32_e32 v84, v84
	v_exp_f32_e32 v85, v85
	ds_read_b128 v[160:163], v210 offset:0
	v_mfma_f32_16x16x32_bf16 v[12:15], v[164:167], v[68:71], v[12:15]
	v_exp_f32_e32 v86, v86
	v_exp_f32_e32 v87, v87
	v_add_f32_e32 v194, v194, v80
	v_mfma_f32_16x16x32_bf16 v[8:11], v[164:167], v[64:67], v[8:11]
	v_add_f32_e32 v194, v194, v81
	v_add_f32_e32 v194, v194, v82
	v_add_f32_e32 v194, v194, v83
	ds_read_b128 v[164:167], v210 offset:2048
	v_mfma_f32_16x16x32_bf16 v[16:19], v[168:171], v[64:67], v[16:19]
	v_add_f32_e32 v195, v195, v84
	v_add_f32_e32 v195, v195, v85
	v_add_f32_e32 v195, v195, v86
	v_mfma_f32_16x16x32_bf16 v[20:23], v[168:171], v[68:71], v[20:23]
	v_add_f32_e32 v195, v195, v87
	v_cvt_pk_bf16_f32 v80, v80, v81
	v_cvt_pk_bf16_f32 v81, v82, v83
	ds_read_b128 v[168:171], v210 offset:4096
	v_mfma_f32_16x16x32_bf16 v[28:31], v[172:175], v[68:71], v[28:31]
	v_cvt_pk_bf16_f32 v84, v84, v85
	v_cvt_pk_bf16_f32 v85, v86, v87
	v_mfma_f32_16x16x32_bf16 v[24:27], v[172:175], v[64:67], v[24:27]
	ds_read_b128 v[172:175], v210 offset:6144
	s_waitcnt lgkmcnt(4)
	v_mfma_f32_16x16x32_bf16 v[32:35], v[176:179], v[64:67], v[32:35]
	v_exp_f32_e32 v88, v88
	v_exp_f32_e32 v89, v89
	v_exp_f32_e32 v90, v90
	v_mfma_f32_16x16x32_bf16 v[36:39], v[176:179], v[68:71], v[36:39]
	v_exp_f32_e32 v91, v91
	v_exp_f32_e32 v92, v92
	v_exp_f32_e32 v93, v93
	ds_read_b128 v[176:179], v210 offset:8192
	v_mfma_f32_16x16x32_bf16 v[44:47], v[180:183], v[68:71], v[44:47]
	v_exp_f32_e32 v94, v94
	v_exp_f32_e32 v95, v95
	v_add_f32_e32 v194, v194, v88
	v_mfma_f32_16x16x32_bf16 v[40:43], v[180:183], v[64:67], v[40:43]
	v_add_f32_e32 v194, v194, v89
	v_add_f32_e32 v194, v194, v90
	v_add_f32_e32 v194, v194, v91
	ds_read_b128 v[180:183], v210 offset:10240
	v_mfma_f32_16x16x32_bf16 v[48:51], v[230:233], v[64:67], v[48:51]
	v_add_f32_e32 v195, v195, v92
	v_add_f32_e32 v195, v195, v93
	v_add_f32_e32 v195, v195, v94
	v_mfma_f32_16x16x32_bf16 v[52:55], v[230:233], v[68:71], v[52:55]
	v_add_f32_e32 v195, v195, v95
	v_cvt_pk_bf16_f32 v82, v88, v89
	v_cvt_pk_bf16_f32 v83, v90, v91
	ds_read_b128 v[230:233], v210 offset:12288
	v_mfma_f32_16x16x32_bf16 v[60:63], v[234:237], v[68:71], v[60:63]
	v_cvt_pk_bf16_f32 v86, v92, v93
	v_cvt_pk_bf16_f32 v87, v94, v95
	v_mfma_f32_16x16x32_bf16 v[56:59], v[234:237], v[64:67], v[56:59]
	ds_read_b128 v[234:237], v210 offset:14336
	s_waitcnt lgkmcnt(7)
	v_mfma_f32_16x16x32_bf16 v[0:3], v[160:163], v[80:83], v[0:3]
	v_mfma_f32_16x16x32_bf16 v[4:7], v[160:163], v[84:87], v[4:7]
	ds_read_b128 v[160:163], v201 offset:16384
	s_waitcnt lgkmcnt(7)
	v_mfma_f32_16x16x32_bf16 v[12:15], v[164:167], v[84:87], v[12:15]
	v_mfma_f32_16x16x32_bf16 v[8:11], v[164:167], v[80:83], v[8:11]
	ds_read_b128 v[164:167], v202 offset:16384
	s_waitcnt lgkmcnt(7)
	v_mfma_f32_16x16x32_bf16 v[16:19], v[168:171], v[80:83], v[16:19]
	v_mfma_f32_16x16x32_bf16 v[20:23], v[168:171], v[84:87], v[20:23]
	ds_read_b128 v[168:171], v203 offset:16384
	s_waitcnt lgkmcnt(7)
	v_mfma_f32_16x16x32_bf16 v[28:31], v[172:175], v[84:87], v[28:31]
	v_mfma_f32_16x16x32_bf16 v[24:27], v[172:175], v[80:83], v[24:27]
	ds_read_b128 v[172:175], v204 offset:16384
	s_waitcnt lgkmcnt(7)
	v_mfma_f32_16x16x32_bf16 v[32:35], v[176:179], v[80:83], v[32:35]
	v_mfma_f32_16x16x32_bf16 v[36:39], v[176:179], v[84:87], v[36:39]
	ds_read_b128 v[176:179], v201 offset:20480
	s_waitcnt lgkmcnt(7)
	v_mfma_f32_16x16x32_bf16 v[44:47], v[180:183], v[84:87], v[44:47]
	v_mfma_f32_16x16x32_bf16 v[40:43], v[180:183], v[80:83], v[40:43]
	ds_read_b128 v[180:183], v202 offset:20480
	s_waitcnt lgkmcnt(7)
	v_mfma_f32_16x16x32_bf16 v[48:51], v[230:233], v[80:83], v[48:51]
	v_mfma_f32_16x16x32_bf16 v[52:55], v[230:233], v[84:87], v[52:55]
	ds_read_b128 v[230:233], v203 offset:20480
	s_waitcnt lgkmcnt(7)
	v_mfma_f32_16x16x32_bf16 v[60:63], v[234:237], v[84:87], v[60:63]
	v_mfma_f32_16x16x32_bf16 v[56:59], v[234:237], v[80:83], v[56:59]
	ds_read_b128 v[234:237], v204 offset:20480
	s_waitcnt lgkmcnt(7)
	v_mfma_f32_16x16x32_bf16 v[64:67], v[160:163], v[96:99], 0
	s_waitcnt lgkmcnt(6)
	v_mfma_f32_16x16x32_bf16 v[64:67], v[164:167], v[100:103], v[64:67]
	s_add_u32 s8, s16, 0x3bc00280
	s_addc_u32 s9, s17, 0
	s_add_u32 s6, s15, 0x23a50000
	s_addc_u32 s7, s14, 0
	s_waitcnt lgkmcnt(5)
	v_mfma_f32_16x16x32_bf16 v[64:67], v[168:171], v[104:107], v[64:67]
	s_waitcnt lgkmcnt(4)
	v_mfma_f32_16x16x32_bf16 v[64:67], v[172:175], v[108:111], v[64:67]
	s_waitcnt vmcnt(4)
	ds_write_b128 v225, v[152:155] offset:49152
	v_mfma_f32_16x16x32_bf16 v[68:71], v[172:175], v[124:127], 0
	ds_read_b128 v[172:175], v204 offset:24576
	v_mfma_f32_16x16x32_bf16 v[68:71], v[168:171], v[120:123], v[68:71]
	ds_read_b128 v[168:171], v203 offset:24576
	ds_write_b128 v226, v[156:159] offset:49152
	v_mfma_f32_16x16x32_bf16 v[68:71], v[164:167], v[116:119], v[68:71]
	ds_read_b128 v[164:167], v202 offset:24576
	v_mfma_f32_16x16x32_bf16 v[68:71], v[160:163], v[112:115], v[68:71]
	ds_read_b128 v[160:163], v201 offset:24576
	ds_write_b64 v227, v[148:149] offset:49152
	s_waitcnt lgkmcnt(10)
	v_mfma_f32_16x16x32_bf16 v[72:75], v[176:179], v[96:99], 0
	s_waitcnt lgkmcnt(9)
	v_mfma_f32_16x16x32_bf16 v[72:75], v[180:183], v[100:103], v[72:75]
	ds_write_b64 v228, v[150:151] offset:49152
	s_waitcnt lgkmcnt(9)
	v_mfma_f32_16x16x32_bf16 v[72:75], v[230:233], v[104:107], v[72:75]
	s_waitcnt lgkmcnt(8)
	v_mfma_f32_16x16x32_bf16 v[72:75], v[234:237], v[108:111], v[72:75]
	ds_write_b64 v229, v[144:145] offset:49152
	v_mfma_f32_16x16x32_bf16 v[76:79], v[234:237], v[124:127], 0
	ds_read_b128 v[234:237], v204 offset:28672
	v_mfma_f32_16x16x32_bf16 v[76:79], v[230:233], v[120:123], v[76:79]
	ds_read_b128 v[230:233], v203 offset:28672
	ds_write_b64 v184, v[146:147] offset:49152
	v_mfma_f32_16x16x32_bf16 v[76:79], v[180:183], v[116:119], v[76:79]
	ds_read_b128 v[180:183], v202 offset:28672
	v_mfma_f32_16x16x32_bf16 v[76:79], v[176:179], v[112:115], v[76:79]
	ds_read_b128 v[176:179], v201 offset:28672
	global_load_dwordx4 v[148:151], v198, s[8:9]
	s_waitcnt lgkmcnt(8)
	v_mfma_f32_16x16x32_bf16 v[80:83], v[160:163], v[96:99], 0
	v_exp_f32_e32 v64, v64
	v_exp_f32_e32 v65, v65
	v_exp_f32_e32 v66, v66
	v_mfma_f32_16x16x32_bf16 v[80:83], v[164:167], v[100:103], v[80:83]
	v_exp_f32_e32 v67, v67
	v_exp_f32_e32 v68, v68
	v_exp_f32_e32 v69, v69
	global_load_dwordx4 v[144:147], v199, s[8:9]
	v_mfma_f32_16x16x32_bf16 v[80:83], v[168:171], v[104:107], v[80:83]
	v_exp_f32_e32 v70, v70
	v_exp_f32_e32 v71, v71
	v_add_f32_e32 v194, v194, v64
	v_mfma_f32_16x16x32_bf16 v[80:83], v[172:175], v[108:111], v[80:83]
	v_add_f32_e32 v194, v194, v65
	v_add_f32_e32 v194, v194, v66
	v_add_f32_e32 v194, v194, v67
	global_load_dwordx4 v[152:155], v196, s[6:7]
	v_mfma_f32_16x16x32_bf16 v[84:87], v[172:175], v[124:127], 0
	v_add_f32_e32 v195, v195, v68
	v_add_f32_e32 v195, v195, v69
	v_add_f32_e32 v195, v195, v70
	ds_read_b128 v[172:175], v209 offset:22528
	v_mfma_f32_16x16x32_bf16 v[84:87], v[168:171], v[120:123], v[84:87]
	v_add_f32_e32 v195, v195, v71
	v_cvt_pk_bf16_f32 v64, v64, v65
	v_cvt_pk_bf16_f32 v65, v66, v67
	ds_read_b128 v[168:171], v209 offset:20480
	global_load_dwordx4 v[156:159], v197, s[6:7]
	v_mfma_f32_16x16x32_bf16 v[84:87], v[164:167], v[116:119], v[84:87]
	v_cvt_pk_bf16_f32 v68, v68, v69
	v_cvt_pk_bf16_f32 v69, v70, v71
	ds_read_b128 v[164:167], v209 offset:18432
	v_mfma_f32_16x16x32_bf16 v[84:87], v[160:163], v[112:115], v[84:87]
	ds_read_b128 v[160:163], v209 offset:16384
	s_waitcnt lgkmcnt(4)
	v_mfma_f32_16x16x32_bf16 v[88:91], v[176:179], v[96:99], 0
	v_exp_f32_e32 v72, v72
	v_exp_f32_e32 v73, v73
	v_exp_f32_e32 v74, v74
	v_mfma_f32_16x16x32_bf16 v[88:91], v[180:183], v[100:103], v[88:91]
	v_exp_f32_e32 v75, v75
	v_exp_f32_e32 v76, v76
	v_exp_f32_e32 v77, v77
	v_mfma_f32_16x16x32_bf16 v[88:91], v[230:233], v[104:107], v[88:91]
	v_exp_f32_e32 v78, v78
	v_exp_f32_e32 v79, v79
	v_add_f32_e32 v194, v194, v72
	v_mfma_f32_16x16x32_bf16 v[88:91], v[234:237], v[108:111], v[88:91]
	v_add_f32_e32 v194, v194, v73
	v_add_f32_e32 v194, v194, v74
	v_add_f32_e32 v194, v194, v75
	v_mfma_f32_16x16x32_bf16 v[92:95], v[234:237], v[124:127], 0
	v_add_f32_e32 v195, v195, v76
	v_add_f32_e32 v195, v195, v77
	v_add_f32_e32 v195, v195, v78
	ds_read_b128 v[234:237], v209 offset:30720
	v_mfma_f32_16x16x32_bf16 v[92:95], v[230:233], v[120:123], v[92:95]
	v_add_f32_e32 v195, v195, v79
	v_cvt_pk_bf16_f32 v66, v72, v73
	v_cvt_pk_bf16_f32 v67, v74, v75
	ds_read_b128 v[230:233], v209 offset:28672
	v_mfma_f32_16x16x32_bf16 v[92:95], v[180:183], v[116:119], v[92:95]
	v_cvt_pk_bf16_f32 v70, v76, v77
	v_cvt_pk_bf16_f32 v71, v78, v79
	ds_read_b128 v[180:183], v209 offset:26624
	v_mfma_f32_16x16x32_bf16 v[92:95], v[176:179], v[112:115], v[92:95]
	ds_read_b128 v[176:179], v209 offset:24576
	s_waitcnt lgkmcnt(4)
	v_mfma_f32_16x16x32_bf16 v[0:3], v[160:163], v[64:67], v[0:3]
	v_exp_f32_e32 v80, v80
	v_exp_f32_e32 v81, v81
	v_exp_f32_e32 v82, v82
	v_mfma_f32_16x16x32_bf16 v[4:7], v[160:163], v[68:71], v[4:7]
	v_exp_f32_e32 v83, v83
	v_exp_f32_e32 v84, v84
	v_exp_f32_e32 v85, v85
	ds_read_b128 v[160:163], v210 offset:16384
	v_mfma_f32_16x16x32_bf16 v[12:15], v[164:167], v[68:71], v[12:15]
	v_exp_f32_e32 v86, v86
	v_exp_f32_e32 v87, v87
	v_add_f32_e32 v194, v194, v80
	v_mfma_f32_16x16x32_bf16 v[8:11], v[164:167], v[64:67], v[8:11]
	v_add_f32_e32 v194, v194, v81
	v_add_f32_e32 v194, v194, v82
	v_add_f32_e32 v194, v194, v83
	ds_read_b128 v[164:167], v210 offset:18432
	v_mfma_f32_16x16x32_bf16 v[16:19], v[168:171], v[64:67], v[16:19]
	v_add_f32_e32 v195, v195, v84
	v_add_f32_e32 v195, v195, v85
	v_add_f32_e32 v195, v195, v86
	v_mfma_f32_16x16x32_bf16 v[20:23], v[168:171], v[68:71], v[20:23]
	v_add_f32_e32 v195, v195, v87
	v_cvt_pk_bf16_f32 v80, v80, v81
	v_cvt_pk_bf16_f32 v81, v82, v83
	ds_read_b128 v[168:171], v210 offset:20480
	v_mfma_f32_16x16x32_bf16 v[28:31], v[172:175], v[68:71], v[28:31]
	v_cvt_pk_bf16_f32 v84, v84, v85
	v_cvt_pk_bf16_f32 v85, v86, v87
	v_mfma_f32_16x16x32_bf16 v[24:27], v[172:175], v[64:67], v[24:27]
	ds_read_b128 v[172:175], v210 offset:22528
	s_waitcnt lgkmcnt(4)
	v_mfma_f32_16x16x32_bf16 v[32:35], v[176:179], v[64:67], v[32:35]
	v_exp_f32_e32 v88, v88
	v_exp_f32_e32 v89, v89
	v_exp_f32_e32 v90, v90
	v_mfma_f32_16x16x32_bf16 v[36:39], v[176:179], v[68:71], v[36:39]
	v_exp_f32_e32 v91, v91
	v_exp_f32_e32 v92, v92
	v_exp_f32_e32 v93, v93
	ds_read_b128 v[176:179], v210 offset:24576
	v_mfma_f32_16x16x32_bf16 v[44:47], v[180:183], v[68:71], v[44:47]
	v_exp_f32_e32 v94, v94
	v_exp_f32_e32 v95, v95
	v_add_f32_e32 v194, v194, v88
	v_mfma_f32_16x16x32_bf16 v[40:43], v[180:183], v[64:67], v[40:43]
	v_add_f32_e32 v194, v194, v89
	v_add_f32_e32 v194, v194, v90
	v_add_f32_e32 v194, v194, v91
	ds_read_b128 v[180:183], v210 offset:26624
	v_mfma_f32_16x16x32_bf16 v[48:51], v[230:233], v[64:67], v[48:51]
	v_add_f32_e32 v195, v195, v92
	v_add_f32_e32 v195, v195, v93
	v_add_f32_e32 v195, v195, v94
	v_mfma_f32_16x16x32_bf16 v[52:55], v[230:233], v[68:71], v[52:55]
	v_add_f32_e32 v195, v195, v95
	v_cvt_pk_bf16_f32 v82, v88, v89
	v_cvt_pk_bf16_f32 v83, v90, v91
	ds_read_b128 v[230:233], v210 offset:28672
	v_mfma_f32_16x16x32_bf16 v[60:63], v[234:237], v[68:71], v[60:63]
	v_cvt_pk_bf16_f32 v86, v92, v93
	v_cvt_pk_bf16_f32 v87, v94, v95
	v_mfma_f32_16x16x32_bf16 v[56:59], v[234:237], v[64:67], v[56:59]
	ds_read_b128 v[234:237], v210 offset:30720
	s_waitcnt lgkmcnt(7)
	v_mfma_f32_16x16x32_bf16 v[0:3], v[160:163], v[80:83], v[0:3]
	v_mfma_f32_16x16x32_bf16 v[4:7], v[160:163], v[84:87], v[4:7]
	s_waitcnt lgkmcnt(6)
	v_mfma_f32_16x16x32_bf16 v[12:15], v[164:167], v[84:87], v[12:15]
	v_mfma_f32_16x16x32_bf16 v[8:11], v[164:167], v[80:83], v[8:11]
	s_waitcnt lgkmcnt(5)
	v_mfma_f32_16x16x32_bf16 v[16:19], v[168:171], v[80:83], v[16:19]
	v_mfma_f32_16x16x32_bf16 v[20:23], v[168:171], v[84:87], v[20:23]
	s_waitcnt lgkmcnt(4)
	v_mfma_f32_16x16x32_bf16 v[28:31], v[172:175], v[84:87], v[28:31]
	v_mfma_f32_16x16x32_bf16 v[24:27], v[172:175], v[80:83], v[24:27]
	s_waitcnt lgkmcnt(3)
	v_mfma_f32_16x16x32_bf16 v[32:35], v[176:179], v[80:83], v[32:35]
	v_mfma_f32_16x16x32_bf16 v[36:39], v[176:179], v[84:87], v[36:39]
	s_waitcnt lgkmcnt(2)
	v_mfma_f32_16x16x32_bf16 v[44:47], v[180:183], v[84:87], v[44:47]
	v_mfma_f32_16x16x32_bf16 v[40:43], v[180:183], v[80:83], v[40:43]
	s_waitcnt lgkmcnt(1)
	v_mfma_f32_16x16x32_bf16 v[48:51], v[230:233], v[80:83], v[48:51]
	v_mfma_f32_16x16x32_bf16 v[52:55], v[230:233], v[84:87], v[52:55]
	s_waitcnt lgkmcnt(0)
	v_mfma_f32_16x16x32_bf16 v[60:63], v[234:237], v[84:87], v[60:63]
	v_mfma_f32_16x16x32_bf16 v[56:59], v[234:237], v[80:83], v[56:59]
	s_waitcnt lgkmcnt(0)
	s_barrier
	ds_read_b128 v[160:163], v201 offset:32768
	ds_read_b128 v[164:167], v202 offset:32768
	ds_read_b128 v[168:171], v203 offset:32768
	ds_read_b128 v[172:175], v204 offset:32768
	ds_read_b128 v[176:179], v201 offset:36864
	ds_read_b128 v[180:183], v202 offset:36864
	ds_read_b128 v[230:233], v203 offset:36864
	ds_read_b128 v[234:237], v204 offset:36864
	s_waitcnt lgkmcnt(7)
	v_mfma_f32_16x16x32_bf16 v[64:67], v[160:163], v[96:99], 0
	s_waitcnt lgkmcnt(6)
	v_mfma_f32_16x16x32_bf16 v[64:67], v[164:167], v[100:103], v[64:67]
	s_add_u32 s8, s16, 0x3bc00300
	s_addc_u32 s9, s17, 0
	s_add_u32 s6, s15, 0x23a60000
	s_addc_u32 s7, s14, 0
	s_waitcnt lgkmcnt(5)
	v_mfma_f32_16x16x32_bf16 v[64:67], v[168:171], v[104:107], v[64:67]
	s_waitcnt lgkmcnt(4)
	v_mfma_f32_16x16x32_bf16 v[64:67], v[172:175], v[108:111], v[64:67]
	s_waitcnt vmcnt(4)
	ds_write_b128 v225, v[136:139] offset:0
	v_mfma_f32_16x16x32_bf16 v[68:71], v[172:175], v[124:127], 0
	ds_read_b128 v[172:175], v204 offset:40960
	v_mfma_f32_16x16x32_bf16 v[68:71], v[168:171], v[120:123], v[68:71]
	ds_read_b128 v[168:171], v203 offset:40960
	ds_write_b128 v226, v[140:143] offset:0
	v_mfma_f32_16x16x32_bf16 v[68:71], v[164:167], v[116:119], v[68:71]
	ds_read_b128 v[164:167], v202 offset:40960
	v_mfma_f32_16x16x32_bf16 v[68:71], v[160:163], v[112:115], v[68:71]
	ds_read_b128 v[160:163], v201 offset:40960
	ds_write_b64 v227, v[132:133] offset:0
	s_waitcnt lgkmcnt(10)
	v_mfma_f32_16x16x32_bf16 v[72:75], v[176:179], v[96:99], 0
	s_waitcnt lgkmcnt(9)
	v_mfma_f32_16x16x32_bf16 v[72:75], v[180:183], v[100:103], v[72:75]
	ds_write_b64 v228, v[134:135] offset:0
	s_waitcnt lgkmcnt(9)
	v_mfma_f32_16x16x32_bf16 v[72:75], v[230:233], v[104:107], v[72:75]
	s_waitcnt lgkmcnt(8)
	v_mfma_f32_16x16x32_bf16 v[72:75], v[234:237], v[108:111], v[72:75]
	ds_write_b64 v229, v[128:129] offset:0
	v_mfma_f32_16x16x32_bf16 v[76:79], v[234:237], v[124:127], 0
	ds_read_b128 v[234:237], v204 offset:45056
	v_mfma_f32_16x16x32_bf16 v[76:79], v[230:233], v[120:123], v[76:79]
	ds_read_b128 v[230:233], v203 offset:45056
	ds_write_b64 v184, v[130:131] offset:0
	v_mfma_f32_16x16x32_bf16 v[76:79], v[180:183], v[116:119], v[76:79]
	ds_read_b128 v[180:183], v202 offset:45056
	v_mfma_f32_16x16x32_bf16 v[76:79], v[176:179], v[112:115], v[76:79]
	ds_read_b128 v[176:179], v201 offset:45056
	global_load_dwordx4 v[132:135], v198, s[8:9]
	s_waitcnt lgkmcnt(8)
	v_mfma_f32_16x16x32_bf16 v[80:83], v[160:163], v[96:99], 0
	v_exp_f32_e32 v64, v64
	v_exp_f32_e32 v65, v65
	v_exp_f32_e32 v66, v66
	v_mfma_f32_16x16x32_bf16 v[80:83], v[164:167], v[100:103], v[80:83]
	v_exp_f32_e32 v67, v67
	v_exp_f32_e32 v68, v68
	v_exp_f32_e32 v69, v69
	global_load_dwordx4 v[128:131], v199, s[8:9]
	v_mfma_f32_16x16x32_bf16 v[80:83], v[168:171], v[104:107], v[80:83]
	v_exp_f32_e32 v70, v70
	v_exp_f32_e32 v71, v71
	v_add_f32_e32 v194, v194, v64
	v_mfma_f32_16x16x32_bf16 v[80:83], v[172:175], v[108:111], v[80:83]
	v_add_f32_e32 v194, v194, v65
	v_add_f32_e32 v194, v194, v66
	v_add_f32_e32 v194, v194, v67
	global_load_dwordx4 v[136:139], v196, s[6:7]
	v_mfma_f32_16x16x32_bf16 v[84:87], v[172:175], v[124:127], 0
	v_add_f32_e32 v195, v195, v68
	v_add_f32_e32 v195, v195, v69
	v_add_f32_e32 v195, v195, v70
	ds_read_b128 v[172:175], v209 offset:38912
	v_mfma_f32_16x16x32_bf16 v[84:87], v[168:171], v[120:123], v[84:87]
	v_add_f32_e32 v195, v195, v71
	v_cvt_pk_bf16_f32 v64, v64, v65
	v_cvt_pk_bf16_f32 v65, v66, v67
	ds_read_b128 v[168:171], v209 offset:36864
	global_load_dwordx4 v[140:143], v197, s[6:7]
	v_mfma_f32_16x16x32_bf16 v[84:87], v[164:167], v[116:119], v[84:87]
	v_cvt_pk_bf16_f32 v68, v68, v69
	v_cvt_pk_bf16_f32 v69, v70, v71
	ds_read_b128 v[164:167], v209 offset:34816
	v_mfma_f32_16x16x32_bf16 v[84:87], v[160:163], v[112:115], v[84:87]
	ds_read_b128 v[160:163], v209 offset:32768
	s_waitcnt lgkmcnt(4)
	v_mfma_f32_16x16x32_bf16 v[88:91], v[176:179], v[96:99], 0
	v_exp_f32_e32 v72, v72
	v_exp_f32_e32 v73, v73
	v_exp_f32_e32 v74, v74
	v_mfma_f32_16x16x32_bf16 v[88:91], v[180:183], v[100:103], v[88:91]
	v_exp_f32_e32 v75, v75
	v_exp_f32_e32 v76, v76
	v_exp_f32_e32 v77, v77
	v_mfma_f32_16x16x32_bf16 v[88:91], v[230:233], v[104:107], v[88:91]
	v_exp_f32_e32 v78, v78
	v_exp_f32_e32 v79, v79
	v_add_f32_e32 v194, v194, v72
	v_mfma_f32_16x16x32_bf16 v[88:91], v[234:237], v[108:111], v[88:91]
	v_add_f32_e32 v194, v194, v73
	v_add_f32_e32 v194, v194, v74
	v_add_f32_e32 v194, v194, v75
	v_mfma_f32_16x16x32_bf16 v[92:95], v[234:237], v[124:127], 0
	v_add_f32_e32 v195, v195, v76
	v_add_f32_e32 v195, v195, v77
	v_add_f32_e32 v195, v195, v78
	ds_read_b128 v[234:237], v209 offset:47104
	v_mfma_f32_16x16x32_bf16 v[92:95], v[230:233], v[120:123], v[92:95]
	v_add_f32_e32 v195, v195, v79
	v_cvt_pk_bf16_f32 v66, v72, v73
	v_cvt_pk_bf16_f32 v67, v74, v75
	ds_read_b128 v[230:233], v209 offset:45056
	v_mfma_f32_16x16x32_bf16 v[92:95], v[180:183], v[116:119], v[92:95]
	v_cvt_pk_bf16_f32 v70, v76, v77
	v_cvt_pk_bf16_f32 v71, v78, v79
	ds_read_b128 v[180:183], v209 offset:43008
	v_mfma_f32_16x16x32_bf16 v[92:95], v[176:179], v[112:115], v[92:95]
	ds_read_b128 v[176:179], v209 offset:40960
	s_waitcnt lgkmcnt(4)
	v_mfma_f32_16x16x32_bf16 v[0:3], v[160:163], v[64:67], v[0:3]
	v_exp_f32_e32 v80, v80
	v_exp_f32_e32 v81, v81
	v_exp_f32_e32 v82, v82
	v_mfma_f32_16x16x32_bf16 v[4:7], v[160:163], v[68:71], v[4:7]
	v_exp_f32_e32 v83, v83
	v_exp_f32_e32 v84, v84
	v_exp_f32_e32 v85, v85
	ds_read_b128 v[160:163], v210 offset:32768
	v_mfma_f32_16x16x32_bf16 v[12:15], v[164:167], v[68:71], v[12:15]
	v_exp_f32_e32 v86, v86
	v_exp_f32_e32 v87, v87
	v_add_f32_e32 v194, v194, v80
	v_mfma_f32_16x16x32_bf16 v[8:11], v[164:167], v[64:67], v[8:11]
	v_add_f32_e32 v194, v194, v81
	v_add_f32_e32 v194, v194, v82
	v_add_f32_e32 v194, v194, v83
	ds_read_b128 v[164:167], v210 offset:34816
	v_mfma_f32_16x16x32_bf16 v[16:19], v[168:171], v[64:67], v[16:19]
	v_add_f32_e32 v195, v195, v84
	v_add_f32_e32 v195, v195, v85
	v_add_f32_e32 v195, v195, v86
	v_mfma_f32_16x16x32_bf16 v[20:23], v[168:171], v[68:71], v[20:23]
	v_add_f32_e32 v195, v195, v87
	v_cvt_pk_bf16_f32 v80, v80, v81
	v_cvt_pk_bf16_f32 v81, v82, v83
	ds_read_b128 v[168:171], v210 offset:36864
	v_mfma_f32_16x16x32_bf16 v[28:31], v[172:175], v[68:71], v[28:31]
	v_cvt_pk_bf16_f32 v84, v84, v85
	v_cvt_pk_bf16_f32 v85, v86, v87
	v_mfma_f32_16x16x32_bf16 v[24:27], v[172:175], v[64:67], v[24:27]
	ds_read_b128 v[172:175], v210 offset:38912
	s_waitcnt lgkmcnt(4)
	v_mfma_f32_16x16x32_bf16 v[32:35], v[176:179], v[64:67], v[32:35]
	v_exp_f32_e32 v88, v88
	v_exp_f32_e32 v89, v89
	v_exp_f32_e32 v90, v90
	v_mfma_f32_16x16x32_bf16 v[36:39], v[176:179], v[68:71], v[36:39]
	v_exp_f32_e32 v91, v91
	v_exp_f32_e32 v92, v92
	v_exp_f32_e32 v93, v93
	ds_read_b128 v[176:179], v210 offset:40960
	v_mfma_f32_16x16x32_bf16 v[44:47], v[180:183], v[68:71], v[44:47]
	v_exp_f32_e32 v94, v94
	v_exp_f32_e32 v95, v95
	v_add_f32_e32 v194, v194, v88
	v_mfma_f32_16x16x32_bf16 v[40:43], v[180:183], v[64:67], v[40:43]
	v_add_f32_e32 v194, v194, v89
	v_add_f32_e32 v194, v194, v90
	v_add_f32_e32 v194, v194, v91
	ds_read_b128 v[180:183], v210 offset:43008
	v_mfma_f32_16x16x32_bf16 v[48:51], v[230:233], v[64:67], v[48:51]
	v_add_f32_e32 v195, v195, v92
	v_add_f32_e32 v195, v195, v93
	v_add_f32_e32 v195, v195, v94
	v_mfma_f32_16x16x32_bf16 v[52:55], v[230:233], v[68:71], v[52:55]
	v_add_f32_e32 v195, v195, v95
	v_cvt_pk_bf16_f32 v82, v88, v89
	v_cvt_pk_bf16_f32 v83, v90, v91
	ds_read_b128 v[230:233], v210 offset:45056
	v_mfma_f32_16x16x32_bf16 v[60:63], v[234:237], v[68:71], v[60:63]
	v_cvt_pk_bf16_f32 v86, v92, v93
	v_cvt_pk_bf16_f32 v87, v94, v95
	v_mfma_f32_16x16x32_bf16 v[56:59], v[234:237], v[64:67], v[56:59]
	ds_read_b128 v[234:237], v210 offset:47104
	s_waitcnt lgkmcnt(7)
	v_mfma_f32_16x16x32_bf16 v[0:3], v[160:163], v[80:83], v[0:3]
	v_mfma_f32_16x16x32_bf16 v[4:7], v[160:163], v[84:87], v[4:7]
	ds_read_b128 v[160:163], v201 offset:49152
	s_waitcnt lgkmcnt(7)
	v_mfma_f32_16x16x32_bf16 v[12:15], v[164:167], v[84:87], v[12:15]
	v_mfma_f32_16x16x32_bf16 v[8:11], v[164:167], v[80:83], v[8:11]
	ds_read_b128 v[164:167], v202 offset:49152
	s_waitcnt lgkmcnt(7)
	v_mfma_f32_16x16x32_bf16 v[16:19], v[168:171], v[80:83], v[16:19]
	v_mfma_f32_16x16x32_bf16 v[20:23], v[168:171], v[84:87], v[20:23]
	ds_read_b128 v[168:171], v203 offset:49152
	s_waitcnt lgkmcnt(7)
	v_mfma_f32_16x16x32_bf16 v[28:31], v[172:175], v[84:87], v[28:31]
	v_mfma_f32_16x16x32_bf16 v[24:27], v[172:175], v[80:83], v[24:27]
	ds_read_b128 v[172:175], v204 offset:49152
	s_waitcnt lgkmcnt(7)
	v_mfma_f32_16x16x32_bf16 v[32:35], v[176:179], v[80:83], v[32:35]
	v_mfma_f32_16x16x32_bf16 v[36:39], v[176:179], v[84:87], v[36:39]
	ds_read_b128 v[176:179], v201 offset:53248
	s_waitcnt lgkmcnt(7)
	v_mfma_f32_16x16x32_bf16 v[44:47], v[180:183], v[84:87], v[44:47]
	v_mfma_f32_16x16x32_bf16 v[40:43], v[180:183], v[80:83], v[40:43]
	ds_read_b128 v[180:183], v202 offset:53248
	s_waitcnt lgkmcnt(7)
	v_mfma_f32_16x16x32_bf16 v[48:51], v[230:233], v[80:83], v[48:51]
	v_mfma_f32_16x16x32_bf16 v[52:55], v[230:233], v[84:87], v[52:55]
	ds_read_b128 v[230:233], v203 offset:53248
	s_waitcnt lgkmcnt(7)
	v_mfma_f32_16x16x32_bf16 v[60:63], v[234:237], v[84:87], v[60:63]
	v_mfma_f32_16x16x32_bf16 v[56:59], v[234:237], v[80:83], v[56:59]
	ds_read_b128 v[234:237], v204 offset:53248
	s_waitcnt lgkmcnt(7)
	v_mfma_f32_16x16x32_bf16 v[64:67], v[160:163], v[96:99], 0
	s_waitcnt lgkmcnt(6)
	v_mfma_f32_16x16x32_bf16 v[64:67], v[164:167], v[100:103], v[64:67]
	s_add_u32 s8, s16, 0x3bc00380
	s_addc_u32 s9, s17, 0
	s_add_u32 s6, s15, 0x23a70000
	s_addc_u32 s7, s14, 0
	s_waitcnt lgkmcnt(5)
	v_mfma_f32_16x16x32_bf16 v[64:67], v[168:171], v[104:107], v[64:67]
	s_waitcnt lgkmcnt(4)
	v_mfma_f32_16x16x32_bf16 v[64:67], v[172:175], v[108:111], v[64:67]
	s_waitcnt vmcnt(4)
	ds_write_b128 v225, v[152:155] offset:16384
	v_mfma_f32_16x16x32_bf16 v[68:71], v[172:175], v[124:127], 0
	ds_read_b128 v[172:175], v204 offset:57344
	v_mfma_f32_16x16x32_bf16 v[68:71], v[168:171], v[120:123], v[68:71]
	ds_read_b128 v[168:171], v203 offset:57344
	ds_write_b128 v226, v[156:159] offset:16384
	v_mfma_f32_16x16x32_bf16 v[68:71], v[164:167], v[116:119], v[68:71]
	ds_read_b128 v[164:167], v202 offset:57344
	v_mfma_f32_16x16x32_bf16 v[68:71], v[160:163], v[112:115], v[68:71]
	ds_read_b128 v[160:163], v201 offset:57344
	ds_write_b64 v227, v[148:149] offset:16384
	s_waitcnt lgkmcnt(10)
	v_mfma_f32_16x16x32_bf16 v[72:75], v[176:179], v[96:99], 0
	s_waitcnt lgkmcnt(9)
	v_mfma_f32_16x16x32_bf16 v[72:75], v[180:183], v[100:103], v[72:75]
	ds_write_b64 v228, v[150:151] offset:16384
	s_waitcnt lgkmcnt(9)
	v_mfma_f32_16x16x32_bf16 v[72:75], v[230:233], v[104:107], v[72:75]
	s_waitcnt lgkmcnt(8)
	v_mfma_f32_16x16x32_bf16 v[72:75], v[234:237], v[108:111], v[72:75]
	ds_write_b64 v229, v[144:145] offset:16384
	v_mfma_f32_16x16x32_bf16 v[76:79], v[234:237], v[124:127], 0
	ds_read_b128 v[234:237], v204 offset:61440
	v_mfma_f32_16x16x32_bf16 v[76:79], v[230:233], v[120:123], v[76:79]
	ds_read_b128 v[230:233], v203 offset:61440
	ds_write_b64 v184, v[146:147] offset:16384
	v_mfma_f32_16x16x32_bf16 v[76:79], v[180:183], v[116:119], v[76:79]
	ds_read_b128 v[180:183], v202 offset:61440
	v_mfma_f32_16x16x32_bf16 v[76:79], v[176:179], v[112:115], v[76:79]
	ds_read_b128 v[176:179], v201 offset:61440
	global_load_dwordx4 v[148:151], v198, s[8:9]
	s_waitcnt lgkmcnt(8)
	v_mfma_f32_16x16x32_bf16 v[80:83], v[160:163], v[96:99], 0
	v_exp_f32_e32 v64, v64
	v_exp_f32_e32 v65, v65
	v_exp_f32_e32 v66, v66
	v_mfma_f32_16x16x32_bf16 v[80:83], v[164:167], v[100:103], v[80:83]
	v_exp_f32_e32 v67, v67
	v_exp_f32_e32 v68, v68
	v_exp_f32_e32 v69, v69
	global_load_dwordx4 v[144:147], v199, s[8:9]
	v_mfma_f32_16x16x32_bf16 v[80:83], v[168:171], v[104:107], v[80:83]
	v_exp_f32_e32 v70, v70
	v_exp_f32_e32 v71, v71
	v_add_f32_e32 v194, v194, v64
	v_mfma_f32_16x16x32_bf16 v[80:83], v[172:175], v[108:111], v[80:83]
	v_add_f32_e32 v194, v194, v65
	v_add_f32_e32 v194, v194, v66
	v_add_f32_e32 v194, v194, v67
	global_load_dwordx4 v[152:155], v196, s[6:7]
	v_mfma_f32_16x16x32_bf16 v[84:87], v[172:175], v[124:127], 0
	v_add_f32_e32 v195, v195, v68
	v_add_f32_e32 v195, v195, v69
	v_add_f32_e32 v195, v195, v70
	ds_read_b128 v[172:175], v209 offset:55296
	v_mfma_f32_16x16x32_bf16 v[84:87], v[168:171], v[120:123], v[84:87]
	v_add_f32_e32 v195, v195, v71
	v_cvt_pk_bf16_f32 v64, v64, v65
	v_cvt_pk_bf16_f32 v65, v66, v67
	ds_read_b128 v[168:171], v209 offset:53248
	global_load_dwordx4 v[156:159], v197, s[6:7]
	v_mfma_f32_16x16x32_bf16 v[84:87], v[164:167], v[116:119], v[84:87]
	v_cvt_pk_bf16_f32 v68, v68, v69
	v_cvt_pk_bf16_f32 v69, v70, v71
	ds_read_b128 v[164:167], v209 offset:51200
	v_mfma_f32_16x16x32_bf16 v[84:87], v[160:163], v[112:115], v[84:87]
	ds_read_b128 v[160:163], v209 offset:49152
	s_waitcnt lgkmcnt(4)
	v_mfma_f32_16x16x32_bf16 v[88:91], v[176:179], v[96:99], 0
	v_exp_f32_e32 v72, v72
	v_exp_f32_e32 v73, v73
	v_exp_f32_e32 v74, v74
	v_mfma_f32_16x16x32_bf16 v[88:91], v[180:183], v[100:103], v[88:91]
	v_exp_f32_e32 v75, v75
	v_exp_f32_e32 v76, v76
	v_exp_f32_e32 v77, v77
	v_mfma_f32_16x16x32_bf16 v[88:91], v[230:233], v[104:107], v[88:91]
	v_exp_f32_e32 v78, v78
	v_exp_f32_e32 v79, v79
	v_add_f32_e32 v194, v194, v72
	v_mfma_f32_16x16x32_bf16 v[88:91], v[234:237], v[108:111], v[88:91]
	v_add_f32_e32 v194, v194, v73
	v_add_f32_e32 v194, v194, v74
	v_add_f32_e32 v194, v194, v75
	v_mfma_f32_16x16x32_bf16 v[92:95], v[234:237], v[124:127], 0
	v_add_f32_e32 v195, v195, v76
	v_add_f32_e32 v195, v195, v77
	v_add_f32_e32 v195, v195, v78
	ds_read_b128 v[234:237], v209 offset:63488
	v_mfma_f32_16x16x32_bf16 v[92:95], v[230:233], v[120:123], v[92:95]
	v_add_f32_e32 v195, v195, v79
	v_cvt_pk_bf16_f32 v66, v72, v73
	v_cvt_pk_bf16_f32 v67, v74, v75
	ds_read_b128 v[230:233], v209 offset:61440
	v_mfma_f32_16x16x32_bf16 v[92:95], v[180:183], v[116:119], v[92:95]
	v_cvt_pk_bf16_f32 v70, v76, v77
	v_cvt_pk_bf16_f32 v71, v78, v79
	ds_read_b128 v[180:183], v209 offset:59392
	v_mfma_f32_16x16x32_bf16 v[92:95], v[176:179], v[112:115], v[92:95]
	ds_read_b128 v[176:179], v209 offset:57344
	s_waitcnt lgkmcnt(4)
	v_mfma_f32_16x16x32_bf16 v[0:3], v[160:163], v[64:67], v[0:3]
	v_exp_f32_e32 v80, v80
	v_exp_f32_e32 v81, v81
	v_exp_f32_e32 v82, v82
	v_mfma_f32_16x16x32_bf16 v[4:7], v[160:163], v[68:71], v[4:7]
	v_exp_f32_e32 v83, v83
	v_exp_f32_e32 v84, v84
	v_exp_f32_e32 v85, v85
	ds_read_b128 v[160:163], v210 offset:49152
	v_mfma_f32_16x16x32_bf16 v[12:15], v[164:167], v[68:71], v[12:15]
	v_exp_f32_e32 v86, v86
	v_exp_f32_e32 v87, v87
	v_add_f32_e32 v194, v194, v80
	v_mfma_f32_16x16x32_bf16 v[8:11], v[164:167], v[64:67], v[8:11]
	v_add_f32_e32 v194, v194, v81
	v_add_f32_e32 v194, v194, v82
	v_add_f32_e32 v194, v194, v83
	ds_read_b128 v[164:167], v210 offset:51200
	v_mfma_f32_16x16x32_bf16 v[16:19], v[168:171], v[64:67], v[16:19]
	v_add_f32_e32 v195, v195, v84
	v_add_f32_e32 v195, v195, v85
	v_add_f32_e32 v195, v195, v86
	v_mfma_f32_16x16x32_bf16 v[20:23], v[168:171], v[68:71], v[20:23]
	v_add_f32_e32 v195, v195, v87
	v_cvt_pk_bf16_f32 v80, v80, v81
	v_cvt_pk_bf16_f32 v81, v82, v83
	ds_read_b128 v[168:171], v210 offset:53248
	v_mfma_f32_16x16x32_bf16 v[28:31], v[172:175], v[68:71], v[28:31]
	v_cvt_pk_bf16_f32 v84, v84, v85
	v_cvt_pk_bf16_f32 v85, v86, v87
	v_mfma_f32_16x16x32_bf16 v[24:27], v[172:175], v[64:67], v[24:27]
	ds_read_b128 v[172:175], v210 offset:55296
	s_waitcnt lgkmcnt(4)
	v_mfma_f32_16x16x32_bf16 v[32:35], v[176:179], v[64:67], v[32:35]
	v_exp_f32_e32 v88, v88
	v_exp_f32_e32 v89, v89
	v_exp_f32_e32 v90, v90
	v_mfma_f32_16x16x32_bf16 v[36:39], v[176:179], v[68:71], v[36:39]
	v_exp_f32_e32 v91, v91
	v_exp_f32_e32 v92, v92
	v_exp_f32_e32 v93, v93
	ds_read_b128 v[176:179], v210 offset:57344
	s_add_u32 s10, s10, 0x200
	s_addc_u32 s11, s11, 0
	s_add_u32 s12, s12, 0x40000
	s_addc_u32 s13, s13, 0
	s_add_i32 s4, s4, 4
	s_cmpk_lt_u32 s4, 0x104
	s_cselect_b64 s[6:7], -1, 0
	s_and_b64 s[6:7], s[0:1], s[6:7]
	s_and_b64 vcc, exec, s[6:7]
	v_mfma_f32_16x16x32_bf16 v[44:47], v[180:183], v[68:71], v[44:47]
	v_exp_f32_e32 v94, v94
	v_exp_f32_e32 v95, v95
	v_add_f32_e32 v194, v194, v88
	v_mfma_f32_16x16x32_bf16 v[40:43], v[180:183], v[64:67], v[40:43]
	v_add_f32_e32 v194, v194, v89
	v_add_f32_e32 v194, v194, v90
	v_add_f32_e32 v194, v194, v91
	ds_read_b128 v[180:183], v210 offset:59392
	v_mfma_f32_16x16x32_bf16 v[48:51], v[230:233], v[64:67], v[48:51]
	v_add_f32_e32 v195, v195, v92
	v_add_f32_e32 v195, v195, v93
	v_add_f32_e32 v195, v195, v94
	v_mfma_f32_16x16x32_bf16 v[52:55], v[230:233], v[68:71], v[52:55]
	v_add_f32_e32 v195, v195, v95
	v_cvt_pk_bf16_f32 v82, v88, v89
	v_cvt_pk_bf16_f32 v83, v90, v91
	ds_read_b128 v[230:233], v210 offset:61440
	v_mfma_f32_16x16x32_bf16 v[60:63], v[234:237], v[68:71], v[60:63]
	v_cvt_pk_bf16_f32 v86, v92, v93
	v_cvt_pk_bf16_f32 v87, v94, v95
	v_mfma_f32_16x16x32_bf16 v[56:59], v[234:237], v[64:67], v[56:59]
	ds_read_b128 v[234:237], v210 offset:63488
	s_waitcnt lgkmcnt(7)
	v_mfma_f32_16x16x32_bf16 v[0:3], v[160:163], v[80:83], v[0:3]
	v_mfma_f32_16x16x32_bf16 v[4:7], v[160:163], v[84:87], v[4:7]
	s_waitcnt lgkmcnt(6)
	v_mfma_f32_16x16x32_bf16 v[12:15], v[164:167], v[84:87], v[12:15]
	v_mfma_f32_16x16x32_bf16 v[8:11], v[164:167], v[80:83], v[8:11]
	s_waitcnt lgkmcnt(5)
	v_mfma_f32_16x16x32_bf16 v[16:19], v[168:171], v[80:83], v[16:19]
	v_mfma_f32_16x16x32_bf16 v[20:23], v[168:171], v[84:87], v[20:23]
	s_waitcnt lgkmcnt(4)
	v_mfma_f32_16x16x32_bf16 v[28:31], v[172:175], v[84:87], v[28:31]
	v_mfma_f32_16x16x32_bf16 v[24:27], v[172:175], v[80:83], v[24:27]
	s_waitcnt lgkmcnt(3)
	v_mfma_f32_16x16x32_bf16 v[32:35], v[176:179], v[80:83], v[32:35]
	v_mfma_f32_16x16x32_bf16 v[36:39], v[176:179], v[84:87], v[36:39]
	s_waitcnt lgkmcnt(2)
	v_mfma_f32_16x16x32_bf16 v[44:47], v[180:183], v[84:87], v[44:47]
	v_mfma_f32_16x16x32_bf16 v[40:43], v[180:183], v[80:83], v[40:43]
	s_waitcnt lgkmcnt(1)
	v_mfma_f32_16x16x32_bf16 v[48:51], v[230:233], v[80:83], v[48:51]
	v_mfma_f32_16x16x32_bf16 v[52:55], v[230:233], v[84:87], v[52:55]
	s_waitcnt lgkmcnt(0)
	v_mfma_f32_16x16x32_bf16 v[60:63], v[234:237], v[84:87], v[60:63]
	v_mfma_f32_16x16x32_bf16 v[56:59], v[234:237], v[80:83], v[56:59]
	s_cbranch_vccnz .LBB0_734
	s_waitcnt vmcnt(0)
	s_nop 7
	s_nop 7
	ds_swizzle_b32 v64, v194 offset:swizzle(SWAP,16)
	s_waitcnt lgkmcnt(0)
	v_add_f32_e32 v194, v194, v64
	v_mov_b32_e32 v65, v194
	s_nop 1
	v_permlane32_swap_b32_e32 v194, v65
	v_add_f32_e32 v194, v194, v65
	s_nop 0
	v_rcp_f32_e32 v66, v194
	ds_swizzle_b32 v64, v195 offset:swizzle(SWAP,16)
	s_waitcnt lgkmcnt(0)
	v_add_f32_e32 v195, v195, v64
	v_mov_b32_e32 v65, v195
	s_nop 1
	v_permlane32_swap_b32_e32 v195, v65
	v_add_f32_e32 v195, v195, v65
	s_nop 0
	v_rcp_f32_e32 v67, v195
	v_readlane_b32 s100, v250, 8
	v_mbcnt_lo_u32_b32 v68, -1, 0
	v_mbcnt_hi_u32_b32 v68, -1, v68
	v_and_b32_e32 v69, 15, v68
	v_lshrrev_b32_e32 v70, 4, v68
	s_lshr_b32 s101, s100, 1
	v_add_u32_e32 v69, s101, v69
	v_lshlrev_b32_e32 v69, 12, v69
	v_and_b32_e32 v71, 1, v70
	v_lshlrev_b32_e32 v71, 5, v71
	v_and_b32_e32 v70, 2, v70
	v_lshl_add_u32 v71, v70, 3, v71
	v_add_u32_e32 v70, v69, v71
	v_add_u32_e32 v71, 0x10000, v70
	v_mul_f32_e32 v0, v0, v66
	v_mul_f32_e32 v1, v1, v66
	v_mul_f32_e32 v2, v2, v66
	v_mul_f32_e32 v3, v3, v66
	v_mul_f32_e32 v8, v8, v66
	v_mul_f32_e32 v9, v9, v66
	v_mul_f32_e32 v10, v10, v66
	v_mul_f32_e32 v11, v11, v66
	v_cvt_pk_bf16_f32 v72, v0, v1
	v_cvt_pk_bf16_f32 v73, v2, v3
	v_cvt_pk_bf16_f32 v74, v8, v9
	v_cvt_pk_bf16_f32 v75, v10, v11
	s_nop 1
	v_permlane16_swap_b32_e32 v72, v74
	v_permlane16_swap_b32_e32 v73, v75
	s_nop 1
	global_store_dwordx4 v70, v[72:75], s[58:59] offset:0
	v_mul_f32_e32 v16, v16, v66
	v_mul_f32_e32 v17, v17, v66
	v_mul_f32_e32 v18, v18, v66
	v_mul_f32_e32 v19, v19, v66
	v_mul_f32_e32 v24, v24, v66
	v_mul_f32_e32 v25, v25, v66
	v_mul_f32_e32 v26, v26, v66
	v_mul_f32_e32 v27, v27, v66
	v_cvt_pk_bf16_f32 v76, v16, v17
	v_cvt_pk_bf16_f32 v77, v18, v19
	v_cvt_pk_bf16_f32 v78, v24, v25
	v_cvt_pk_bf16_f32 v79, v26, v27
	s_nop 1
	v_permlane16_swap_b32_e32 v76, v78
	v_permlane16_swap_b32_e32 v77, v79
	s_nop 1
	global_store_dwordx4 v70, v[76:79], s[58:59] offset:64
	v_mul_f32_e32 v32, v32, v66
	v_mul_f32_e32 v33, v33, v66
	v_mul_f32_e32 v34, v34, v66
	v_mul_f32_e32 v35, v35, v66
	v_mul_f32_e32 v40, v40, v66
	v_mul_f32_e32 v41, v41, v66
	v_mul_f32_e32 v42, v42, v66
	v_mul_f32_e32 v43, v43, v66
	v_cvt_pk_bf16_f32 v80, v32, v33
	v_cvt_pk_bf16_f32 v81, v34, v35
	v_cvt_pk_bf16_f32 v82, v40, v41
	v_cvt_pk_bf16_f32 v83, v42, v43
	s_nop 1
	v_permlane16_swap_b32_e32 v80, v82
	v_permlane16_swap_b32_e32 v81, v83
	s_nop 1
	global_store_dwordx4 v70, v[80:83], s[58:59] offset:128
	v_mul_f32_e32 v48, v48, v66
	v_mul_f32_e32 v49, v49, v66
	v_mul_f32_e32 v50, v50, v66
	v_mul_f32_e32 v51, v51, v66
	v_mul_f32_e32 v56, v56, v66
	v_mul_f32_e32 v57, v57, v66
	v_mul_f32_e32 v58, v58, v66
	v_mul_f32_e32 v59, v59, v66
	v_cvt_pk_bf16_f32 v84, v48, v49
	v_cvt_pk_bf16_f32 v85, v50, v51
	v_cvt_pk_bf16_f32 v86, v56, v57
	v_cvt_pk_bf16_f32 v87, v58, v59
	s_nop 1
	v_permlane16_swap_b32_e32 v84, v86
	v_permlane16_swap_b32_e32 v85, v87
	s_nop 1
	global_store_dwordx4 v70, v[84:87], s[58:59] offset:192
	v_mul_f32_e32 v4, v4, v67
	v_mul_f32_e32 v5, v5, v67
	v_mul_f32_e32 v6, v6, v67
	v_mul_f32_e32 v7, v7, v67
	v_mul_f32_e32 v12, v12, v67
	v_mul_f32_e32 v13, v13, v67
	v_mul_f32_e32 v14, v14, v67
	v_mul_f32_e32 v15, v15, v67
	v_cvt_pk_bf16_f32 v88, v4, v5
	v_cvt_pk_bf16_f32 v89, v6, v7
	v_cvt_pk_bf16_f32 v90, v12, v13
	v_cvt_pk_bf16_f32 v91, v14, v15
	s_nop 1
	v_permlane16_swap_b32_e32 v88, v90
	v_permlane16_swap_b32_e32 v89, v91
	s_nop 1
	global_store_dwordx4 v71, v[88:91], s[58:59] offset:0
	v_mul_f32_e32 v20, v20, v67
	v_mul_f32_e32 v21, v21, v67
	v_mul_f32_e32 v22, v22, v67
	v_mul_f32_e32 v23, v23, v67
	v_mul_f32_e32 v28, v28, v67
	v_mul_f32_e32 v29, v29, v67
	v_mul_f32_e32 v30, v30, v67
	v_mul_f32_e32 v31, v31, v67
	v_cvt_pk_bf16_f32 v92, v20, v21
	v_cvt_pk_bf16_f32 v93, v22, v23
	v_cvt_pk_bf16_f32 v94, v28, v29
	v_cvt_pk_bf16_f32 v95, v30, v31
	s_nop 1
	v_permlane16_swap_b32_e32 v92, v94
	v_permlane16_swap_b32_e32 v93, v95
	s_nop 1
	global_store_dwordx4 v71, v[92:95], s[58:59] offset:64
	v_mul_f32_e32 v36, v36, v67
	v_mul_f32_e32 v37, v37, v67
	v_mul_f32_e32 v38, v38, v67
	v_mul_f32_e32 v39, v39, v67
	v_mul_f32_e32 v44, v44, v67
	v_mul_f32_e32 v45, v45, v67
	v_mul_f32_e32 v46, v46, v67
	v_mul_f32_e32 v47, v47, v67
	v_cvt_pk_bf16_f32 v72, v36, v37
	v_cvt_pk_bf16_f32 v73, v38, v39
	v_cvt_pk_bf16_f32 v74, v44, v45
	v_cvt_pk_bf16_f32 v75, v46, v47
	s_nop 1
	v_permlane16_swap_b32_e32 v72, v74
	v_permlane16_swap_b32_e32 v73, v75
	s_nop 1
	global_store_dwordx4 v71, v[72:75], s[58:59] offset:128
	v_mul_f32_e32 v52, v52, v67
	v_mul_f32_e32 v53, v53, v67
	v_mul_f32_e32 v54, v54, v67
	v_mul_f32_e32 v55, v55, v67
	v_mul_f32_e32 v60, v60, v67
	v_mul_f32_e32 v61, v61, v67
	v_mul_f32_e32 v62, v62, v67
	v_mul_f32_e32 v63, v63, v67
	v_cvt_pk_bf16_f32 v76, v52, v53
	v_cvt_pk_bf16_f32 v77, v54, v55
	v_cvt_pk_bf16_f32 v78, v60, v61
	v_cvt_pk_bf16_f32 v79, v62, v63
	s_nop 1
	v_permlane16_swap_b32_e32 v76, v78
	v_permlane16_swap_b32_e32 v77, v79
	s_nop 1
	global_store_dwordx4 v71, v[76:79], s[58:59] offset:192
	s_barrier
